# MLA tile loop: QK^T issued before P.V in the MFMA block, reference subtraction moved from the softmax block into P.V MFMA gaps
# speedup vs baseline: 1.0179x; 1.0115x over previous
.LBB0_1037:
	s_sub_i32 s14, s82, 63
	s_cmp_le_i32 s14, s77
	s_cselect_b64 s[4:5], -1, 0
	s_add_i32 s83, s86, 1
	s_cmp_gt_i32 s14, s77
	s_cbranch_scc1 .LBB0_1045
	s_cmp_le_i32 s82, s0
	s_cbranch_scc1 .LBB0_1042
	v_mov_b32_e32 v90, v122
	s_nop 0
	v_cmp_gt_i32_e64 s[70:71], 26, v90
	v_cmp_gt_i32_e64 s[72:73], 27, v90
	v_cmp_gt_i32_e64 s[68:69], 25, v90
	s_and_b64 s[70:71], s[72:73], s[70:71]
	v_cmp_gt_i32_e64 s[66:67], 24, v90
	s_and_b64 s[68:69], s[70:71], s[68:69]
	v_cmp_gt_i32_e64 s[64:65], 19, v90
	s_and_b64 s[66:67], s[68:69], s[66:67]
	v_cmp_gt_i32_e64 s[62:63], 18, v90
	s_and_b64 s[64:65], s[66:67], s[64:65]
	v_cmp_gt_i32_e64 s[60:61], 17, v90
	s_and_b64 s[62:63], s[64:65], s[62:63]
	v_cmp_gt_i32_e64 s[58:59], 16, v90
	s_and_b64 s[60:61], s[62:63], s[60:61]
	v_cmp_gt_i32_e64 s[56:57], 11, v90
	s_and_b64 s[58:59], s[60:61], s[58:59]
	v_cmp_gt_i32_e64 s[54:55], 10, v90
	s_and_b64 s[56:57], s[58:59], s[56:57]
	v_cmp_gt_i32_e64 s[52:53], 9, v90
	s_and_b64 s[54:55], s[56:57], s[54:55]
	v_cmp_gt_i32_e64 s[50:51], 8, v90
	s_and_b64 s[52:53], s[54:55], s[52:53]
	v_cmp_gt_i32_e64 s[48:49], 3, v90
	s_and_b64 s[50:51], s[52:53], s[50:51]
	v_cmp_gt_i32_e64 s[46:47], 2, v90
	s_and_b64 s[48:49], s[50:51], s[48:49]
	v_cmp_gt_i32_e64 s[44:45], 1, v90
	s_and_b64 s[46:47], s[48:49], s[46:47]
	v_cmp_gt_i32_e64 s[42:43], 0, v90
	s_and_b64 s[44:45], s[46:47], s[44:45]
	s_and_b64 s[42:43], s[44:45], s[42:43]
	v_cmp_gt_i32_e64 s[40:41], 58, v90
	v_cndmask_b32_e64 v50, v50, v240, s[42:43]
	v_cmp_gt_i32_e64 s[42:43], 59, v90
	v_cmp_gt_i32_e64 s[38:39], 57, v90
	s_and_b64 s[40:41], s[42:43], s[40:41]
	v_cmp_gt_i32_e64 s[36:37], 56, v90
	s_and_b64 s[38:39], s[40:41], s[38:39]
	v_cmp_gt_i32_e64 s[34:35], 51, v90
	s_and_b64 s[36:37], s[38:39], s[36:37]
	v_cmp_gt_i32_e64 s[30:31], 50, v90
	s_and_b64 s[34:35], s[36:37], s[34:35]
	v_cmp_gt_i32_e64 s[28:29], 49, v90
	s_and_b64 s[30:31], s[34:35], s[30:31]
	v_cmp_gt_i32_e64 s[26:27], 48, v90
	s_and_b64 s[28:29], s[30:31], s[28:29]
	v_cmp_gt_i32_e64 s[24:25], 43, v90
	s_and_b64 s[26:27], s[28:29], s[26:27]
	v_cmp_gt_i32_e64 s[22:23], 42, v90
	s_and_b64 s[24:25], s[26:27], s[24:25]
	v_cmp_gt_i32_e64 s[20:21], 41, v90
	s_and_b64 s[22:23], s[24:25], s[22:23]
	v_cmp_gt_i32_e64 s[18:19], 40, v90
	s_and_b64 s[20:21], s[22:23], s[20:21]
	v_cmp_gt_i32_e64 s[16:17], 35, v90
	s_and_b64 s[18:19], s[20:21], s[18:19]
	v_cmp_gt_i32_e64 s[14:15], 34, v90
	s_and_b64 s[16:17], s[18:19], s[16:17]
	v_cmp_gt_i32_e64 s[12:13], 33, v90
	s_and_b64 s[14:15], s[16:17], s[14:15]
	v_cmp_gt_i32_e32 vcc, 32, v90
	s_and_b64 s[12:13], s[14:15], s[12:13]
	s_and_b64 vcc, s[12:13], vcc
	v_cndmask_b32_e64 v65, v65, v240, s[72:73]
	v_cndmask_b32_e64 v64, v64, v240, s[70:71]
	v_cndmask_b32_e64 v63, v63, v240, s[68:69]
	v_cndmask_b32_e64 v62, v62, v240, s[66:67]
	v_cndmask_b32_e64 v61, v61, v240, s[64:65]
	s_mov_b64 s[64:65], 0x1f040080
	v_cndmask_b32_e64 v60, v60, v240, s[62:63]
	v_cndmask_b32_e64 v59, v59, v240, s[60:61]
	v_cndmask_b32_e64 v58, v58, v240, s[58:59]
	s_mov_b64 s[58:59], 0x2000
	v_cndmask_b32_e64 v57, v57, v240, s[56:57]
	v_cndmask_b32_e64 v56, v56, v240, s[54:55]
	v_cndmask_b32_e64 v55, v55, v240, s[52:53]
	v_cndmask_b32_e64 v54, v54, v240, s[50:51]
	v_cndmask_b32_e64 v53, v53, v240, s[48:49]
	v_cndmask_b32_e64 v52, v52, v240, s[46:47]
	v_cndmask_b32_e64 v51, v51, v240, s[44:45]
	v_cndmask_b32_e64 v49, v49, v240, s[42:43]
	v_cndmask_b32_e64 v48, v48, v240, s[40:41]
	v_cndmask_b32_e64 v47, v47, v240, s[38:39]
	v_cndmask_b32_e64 v46, v46, v240, s[36:37]
	v_cndmask_b32_e64 v45, v45, v240, s[34:35]
	v_cndmask_b32_e64 v44, v44, v240, s[30:31]
	v_cndmask_b32_e64 v43, v43, v240, s[28:29]
	v_cndmask_b32_e64 v42, v42, v240, s[26:27]
	v_cndmask_b32_e64 v41, v41, v240, s[24:25]
	v_cndmask_b32_e64 v40, v40, v240, s[22:23]
	v_cndmask_b32_e64 v39, v39, v240, s[20:21]
	v_cndmask_b32_e64 v38, v38, v240, s[18:19]
	v_cndmask_b32_e64 v37, v37, v240, s[16:17]
	v_cndmask_b32_e64 v36, v36, v240, s[14:15]
	v_cndmask_b32_e64 v35, v35, v240, s[12:13]
	v_cndmask_b32_e32 v34, v34, v240, vcc

.LBB0_1048:
	s_and_b32 s4, s80, 0x6000
	v_add_u32_e32 v125, s4, v121
	s_cmp_ge_u32 s86, s84
	s_cselect_b64 s[4:5], -1, 0
	s_sub_i32 s12, s82, 30
	s_cmp_gt_i32 s12, s0
	s_cselect_b64 s[12:13], -1, 0
	s_or_b64 s[4:5], s[4:5], s[12:13]
	s_and_b64 vcc, exec, s[4:5]
	s_cbranch_vccnz .Lmla_pv
	s_and_b32 s4, s86, 3
	s_mulk_i32 s4, 0x3000
	v_add_u32_e32 v142, s4, v107
	ds_read_b128 v[144:147], v142
	ds_read_b128 v[148:151], v142 offset:512
	ds_read_b128 v[152:155], v142 offset:2048
	ds_read_b128 v[156:159], v142 offset:2560
	ds_read_b128 v[160:163], v142 offset:4096
	ds_read_b128 v[164:167], v142 offset:4608
	ds_read_b128 v[168:171], v142 offset:6144
	ds_read_b128 v[172:175], v142 offset:6656
	s_waitcnt lgkmcnt(7)
	v_mfma_f32_32x32x16_bf16 v[50:65], v[144:147], v[66:69], 0
	s_waitcnt lgkmcnt(6)
	v_mfma_f32_32x32x16_bf16 v[34:49], v[148:151], v[66:69], 0
	ds_read_b128 v[176:179], v142 offset:8192
	ds_read_b128 v[180:183], v142 offset:8704
	s_waitcnt lgkmcnt(7)
	v_mfma_f32_32x32x16_bf16 v[50:65], v[152:155], v[70:73], v[50:65]
	s_waitcnt lgkmcnt(6)
	v_mfma_f32_32x32x16_bf16 v[34:49], v[156:159], v[70:73], v[34:49]
	ds_read_b128 v[188:191], v142 offset:10240
	ds_read_b128 v[192:195], v142 offset:10752
	s_waitcnt lgkmcnt(7)
	v_mfma_f32_32x32x16_bf16 v[50:65], v[160:163], v[74:77], v[50:65]
	s_waitcnt lgkmcnt(6)
	v_mfma_f32_32x32x16_bf16 v[34:49], v[164:167], v[74:77], v[34:49]
	ds_read_b64_tr_b16 v[126:127], v125 offset:0
	ds_read_b64_tr_b16 v[128:129], v125 offset:0x400
	ds_read_b64_tr_b16 v[130:131], v125 offset:0x200
	ds_read_b64_tr_b16 v[132:133], v125 offset:0x600
	s_waitcnt lgkmcnt(9)
	v_mfma_f32_32x32x16_bf16 v[50:65], v[168:171], v[78:81], v[50:65]
	s_waitcnt lgkmcnt(8)
	v_mfma_f32_32x32x16_bf16 v[34:49], v[172:175], v[78:81], v[34:49]
	ds_read_b64_tr_b16 v[134:135], v125 offset:0x800
	ds_read_b64_tr_b16 v[136:137], v125 offset:0xc00
	ds_read_b64_tr_b16 v[138:139], v125 offset:0xa00
	ds_read_b64_tr_b16 v[140:141], v125 offset:0xe00
	s_waitcnt lgkmcnt(11)
	v_mfma_f32_32x32x16_bf16 v[50:65], v[176:179], v[82:85], v[50:65]
	s_waitcnt lgkmcnt(10)
	v_mfma_f32_32x32x16_bf16 v[34:49], v[180:183], v[82:85], v[34:49]
	s_waitcnt lgkmcnt(9)
	v_mfma_f32_32x32x16_bf16 v[50:65], v[188:191], v[86:89], v[50:65]
	s_waitcnt lgkmcnt(8)
	v_mfma_f32_32x32x16_bf16 v[34:49], v[192:195], v[86:89], v[34:49]
	s_branch .Lmla_pv_mfma
.Lmla_pv:
	ds_read_b64_tr_b16 v[126:127], v125 offset:0
	ds_read_b64_tr_b16 v[128:129], v125 offset:0x400
	ds_read_b64_tr_b16 v[130:131], v125 offset:0x200
	ds_read_b64_tr_b16 v[132:133], v125 offset:0x600
	ds_read_b64_tr_b16 v[134:135], v125 offset:0x800
	ds_read_b64_tr_b16 v[136:137], v125 offset:0xc00
	ds_read_b64_tr_b16 v[138:139], v125 offset:0xa00
	ds_read_b64_tr_b16 v[140:141], v125 offset:0xe00
.Lmla_pv_mfma:
	s_waitcnt lgkmcnt(4)
	s_nop 0
	v_mfma_f32_32x32x16_bf16 v[18:33], v[90:93], v[126:129], v[18:33]
	v_mfma_f32_32x32x16_bf16 v[2:17], v[90:93], v[130:133], v[2:17]
	ds_read_b64_tr_b16 v[126:127], v125 offset:0x1000
	ds_read_b64_tr_b16 v[128:129], v125 offset:0x1400
	ds_read_b64_tr_b16 v[130:131], v125 offset:0x1200
	ds_read_b64_tr_b16 v[132:133], v125 offset:0x1600
	s_waitcnt lgkmcnt(4)
	v_mfma_f32_32x32x16_bf16 v[18:33], v[94:97], v[134:137], v[18:33]
	v_mfma_f32_32x32x16_bf16 v[2:17], v[94:97], v[138:141], v[2:17]
	ds_read_b64_tr_b16 v[134:135], v125 offset:0x1800
	ds_read_b64_tr_b16 v[136:137], v125 offset:0x1c00
	ds_read_b64_tr_b16 v[138:139], v125 offset:0x1a00
	ds_read_b64_tr_b16 v[140:141], v125 offset:0x1e00
	s_waitcnt lgkmcnt(4)
	v_mfma_f32_32x32x16_bf16 v[18:33], v[98:101], v[126:129], v[18:33]
	v_sub_f32_e32 v65, v65, v123
	v_sub_f32_e32 v64, v64, v123
	v_sub_f32_e32 v63, v63, v123
	v_sub_f32_e32 v62, v62, v123
	v_sub_f32_e32 v61, v61, v123
	v_sub_f32_e32 v60, v60, v123
	v_sub_f32_e32 v59, v59, v123
	v_sub_f32_e32 v58, v58, v123
	v_mfma_f32_32x32x16_bf16 v[2:17], v[98:101], v[130:133], v[2:17]
	v_sub_f32_e32 v57, v57, v123
	v_sub_f32_e32 v56, v56, v123
	v_sub_f32_e32 v55, v55, v123
	v_sub_f32_e32 v54, v54, v123
	v_sub_f32_e32 v53, v53, v123
	v_sub_f32_e32 v52, v52, v123
	v_sub_f32_e32 v51, v51, v123
	v_sub_f32_e32 v50, v50, v123
	s_waitcnt lgkmcnt(0)
	v_mfma_f32_32x32x16_bf16 v[18:33], v[102:105], v[134:137], v[18:33]
	v_sub_f32_e32 v49, v49, v123
	v_sub_f32_e32 v48, v48, v123
	v_sub_f32_e32 v47, v47, v123
	v_sub_f32_e32 v46, v46, v123
	v_sub_f32_e32 v45, v45, v123
	v_sub_f32_e32 v44, v44, v123
	v_sub_f32_e32 v43, v43, v123
	v_sub_f32_e32 v42, v42, v123
	v_mfma_f32_32x32x16_bf16 v[2:17], v[102:105], v[138:141], v[2:17]
	v_sub_f32_e32 v41, v41, v123
	v_sub_f32_e32 v40, v40, v123
	v_sub_f32_e32 v39, v39, v123
	v_sub_f32_e32 v38, v38, v123
	v_sub_f32_e32 v37, v37, v123
	v_sub_f32_e32 v36, v36, v123
	v_sub_f32_e32 v35, v35, v123
	v_sub_f32_e32 v34, v34, v123

.Lmla_dma_v3:
	s_add_i32 s12, s86, 2
	s_min_i32 s12, s12, s78
	s_ashr_i32 s13, s12, 31
	s_add_i32 s15, s80, 0x6000
	s_lshl_b64 s[12:13], s[12:13], 16
	s_and_b32 s15, s15, 0x6000
	v_readlane_b32 s16, v254, 34
	s_add_i32 s15, s15, s16
	v_lshl_add_u64 v[196:197], v[114:115], 0, s[12:13]
	s_mov_b32 s12, m0
	s_mov_b32 m0, s15
	s_nop 0
	global_load_lds_dwordx4 v[196:197], off
	s_mov_b32 m0, s12
	s_and_b64 vcc, exec, s[6:7]
	s_cbranch_vccz .LBB0_1056

.LBB0_1053:
	s_add_i32 s4, s81, s83
	s_addk_i32 s80, 0x2000
	s_add_i32 s82, s82, 64
	s_cmp_eq_u32 s4, 1
	v_subrev_u32_e32 v122, 64, v122
	s_cbranch_scc1 .LBB0_1069
	s_mov_b32 s86, s83
	s_branch .LBB0_1037
.LBB0_1056:
	s_waitcnt vmcnt(4) lgkmcnt(0)
	s_barrier
	s_cbranch_execz .LBB0_1052
	s_branch .LBB0_1053
